# fp8 V^T blocks stored with the two 32-key halves of a lane interleaved, so the sel tile reads its PV operands with 8 ds_read_b128 instead of 16 ds_read_b64
# speedup vs baseline: 1.0070x; 1.0070x over previous
; #define GAS __attribute__((address_space(1)))
; __device__ __forceinline__ unsigned pk4_fp8(float a, float b, float c, float d) { unsigned w = 0u; w = __builtin_amdgcn_cvt_pk_fp8_f32(a, b, w, false); w = __builtin_amdgcn_cvt_pk_fp8_f32(c, d, w, true); return w; }
; __device__ __forceinline__ void vt8_transpose(Frame& F) {
;     ...
;     for (int blk = gw; blk < 2048; blk += NGW) {
;         const GAS unsigned* src = (const GAS unsigned*)(VSu + (size_t)blk * 64 * 64) + F.lane;
;         unsigned v[64];
; #pragma unroll
;         for (int t = 0; t < 64; ++t) v[t] = src[t * 64];
;         u32x4 lo[4], hi[4];
; #pragma unroll
;         for (int w = 0; w < 16; ++w) { const int k0 = 32 * (w >> 3) + 16 * (w & 1) + 4 * ((w & 7) >> 1);
;             lo[w >> 2][w & 3] = pk4_fp8(bf_lo(v[k0]), bf_lo(v[k0 + 1]), bf_lo(v[k0 + 2]), bf_lo(v[k0 + 3])); hi[w >> 2][w & 3] = pk4_fp8(bf_hi(v[k0]), bf_hi(v[k0 + 1]), bf_hi(v[k0 + 2]), bf_hi(v[k0 + 3])); }
;         GAS u32x4* dst = (GAS u32x4*)(VT + (size_t)blk * 8192 + (size_t)(2 * F.lane) * 64);
; #pragma unroll
;         for (int j = 0; j < 4; ++j) { dst[j] = lo[j]; dst[4 + j] = hi[j]; }
.LBB0_1426:
	v_lshl_add_u64 v[38:39], s[28:29], 0, v[36:37]
	v_add_co_u32_e64 v44, s[2:3], s5, v38
	v_add_co_u32_e32 v42, vcc, 0x28000000, v38
	s_nop 0
	v_addc_co_u32_e64 v45, s[2:3], 0, v39, s[2:3]
	v_add_co_u32_e64 v46, s[2:3], s7, v38
	v_addc_co_u32_e32 v43, vcc, 0, v39, vcc
	s_nop 0
	v_addc_co_u32_e64 v47, s[2:3], 0, v39, s[2:3]
	v_add_co_u32_e64 v48, s[2:3], s14, v38
	global_load_dword v33, v[46:47], off offset:-4096
	global_load_dword v38, v[44:45], off offset:256
	global_load_dword v50, v[44:45], off offset:512
	global_load_dword v51, v[44:45], off offset:768
	global_load_dword v52, v[44:45], off offset:1024
	global_load_dword v53, v[44:45], off offset:1280
	global_load_dword v54, v[44:45], off offset:1536
	global_load_dword v55, v[44:45], off offset:1792
	global_load_dword v56, v[44:45], off offset:2048
	global_load_dword v57, v[44:45], off offset:2304
	global_load_dword v58, v[44:45], off offset:2560
	global_load_dword v59, v[44:45], off offset:2816
	global_load_dword v60, v[44:45], off offset:3072
	global_load_dword v61, v[44:45], off offset:3328
	global_load_dword v62, v[44:45], off offset:3584
	s_nop 0
	global_load_dword v44, v[44:45], off offset:3840
	v_addc_co_u32_e64 v49, s[2:3], 0, v39, s[2:3]
	global_load_dword v39, v[46:47], off
	global_load_dword v45, v[46:47], off offset:256
	global_load_dword v63, v[46:47], off offset:512
	global_load_dword v64, v[46:47], off offset:768
	global_load_dword v65, v[46:47], off offset:1024
	global_load_dword v66, v[46:47], off offset:1280
	global_load_dword v67, v[46:47], off offset:1536
	global_load_dword v68, v[46:47], off offset:1792
	global_load_dword v69, v[48:49], off
	global_load_dword v70, v[48:49], off offset:256
	global_load_dword v71, v[48:49], off offset:512
	global_load_dword v72, v[48:49], off offset:768
	global_load_dword v73, v[46:47], off offset:2048
	global_load_dword v74, v[46:47], off offset:2304
	global_load_dword v75, v[46:47], off offset:2560
	global_load_dword v76, v[46:47], off offset:2816
	global_load_dword v77, v[46:47], off offset:3072
	global_load_dword v78, v[46:47], off offset:3328
	global_load_dword v79, v[46:47], off offset:3584
	global_load_dword v80, v[46:47], off offset:3840
	global_load_dword v81, v[48:49], off offset:1024
	global_load_dword v82, v[48:49], off offset:1280
	global_load_dword v83, v[48:49], off offset:1536
	global_load_dword v84, v[48:49], off offset:1792
	global_load_dword v85, v[48:49], off offset:2048
	global_load_dword v86, v[48:49], off offset:2304
	global_load_dword v87, v[48:49], off offset:2560
	global_load_dword v88, v[48:49], off offset:2816
	global_load_dword v89, v[48:49], off offset:3072
	global_load_dword v90, v[48:49], off offset:3328
	global_load_dword v46, v[48:49], off offset:3584
	global_load_dword v47, v[48:49], off offset:3840
	global_load_dword v91, v[42:43], off
	global_load_dword v92, v[42:43], off offset:256
	global_load_dword v93, v[42:43], off offset:512
	global_load_dword v94, v[42:43], off offset:768
	global_load_dword v95, v[42:43], off offset:1024
	global_load_dword v96, v[42:43], off offset:1280
	global_load_dword v97, v[42:43], off offset:1536
	global_load_dword v98, v[42:43], off offset:1792
	global_load_dword v99, v[42:43], off offset:2048
	global_load_dword v100, v[42:43], off offset:2304
	global_load_dword v101, v[42:43], off offset:2560
	global_load_dword v102, v[42:43], off offset:2816
	global_load_dword v103, v[42:43], off offset:3072
	global_load_dword v48, v[42:43], off offset:3328
	global_load_dword v49, v[42:43], off offset:3584
	global_load_dword v104, v[42:43], off offset:3840
	v_mov_b32_e32 v16, 0
	v_mov_b32_e32 v17, 0
	v_mov_b32_e32 v18, 0
	v_mov_b32_e32 v19, 0
	v_mov_b32_e32 v20, 0
	v_mov_b32_e32 v21, 0
	v_mov_b32_e32 v22, 0
	v_mov_b32_e32 v23, 0
	v_mov_b32_e32 v24, 0
	v_mov_b32_e32 v25, 0
	v_mov_b32_e32 v26, 0
	v_mov_b32_e32 v27, 0
	v_mov_b32_e32 v5, 0
	v_mov_b32_e32 v7, 0
	v_mov_b32_e32 v13, 0
	v_mov_b32_e32 v28, 0
	v_mov_b32_e32 v29, 0
	v_mov_b32_e32 v30, 0
	v_mov_b32_e32 v31, 0
	v_mov_b32_e32 v0, 0
	v_mov_b32_e32 v4, 0
	v_mov_b32_e32 v1, 0
	v_mov_b32_e32 v2, 0
	v_mov_b32_e32 v6, 0
	v_mov_b32_e32 v3, 0
	v_mov_b32_e32 v8, 0
	v_mov_b32_e32 v12, 0
	v_mov_b32_e32 v9, 0
	v_mov_b32_e32 v10, 0
	v_mov_b32_e32 v14, 0
	s_waitcnt vmcnt(47)
	v_lshlrev_b32_e32 v119, 16, v39
	s_waitcnt vmcnt(46)
	v_lshlrev_b32_e32 v120, 16, v45
	v_and_b32_e32 v39, 0xffff0000, v39
	v_and_b32_e32 v45, 0xffff0000, v45
	s_waitcnt vmcnt(43)
	v_lshlrev_b32_e32 v127, 16, v65
	s_waitcnt vmcnt(42)
	v_lshlrev_b32_e32 v128, 16, v66
	v_and_b32_e32 v65, 0xffff0000, v65
	v_and_b32_e32 v66, 0xffff0000, v66
	s_waitcnt vmcnt(39)
	v_lshlrev_b32_e32 v123, 16, v69
	s_waitcnt vmcnt(38)
	v_lshlrev_b32_e32 v124, 16, v70
	v_and_b32_e32 v69, 0xffff0000, v69
	v_and_b32_e32 v70, 0xffff0000, v70
	v_cvt_pk_fp8_f32 v16, v119, v120
	v_cvt_pk_fp8_f32 v17, v123, v124
	v_cvt_pk_fp8_f32 v18, v127, v128
	s_waitcnt vmcnt(35)
	v_lshlrev_b32_e32 v135, 16, v73
	s_waitcnt vmcnt(34)
	v_lshlrev_b32_e32 v136, 16, v74
	s_waitcnt vmcnt(31)
	v_lshlrev_b32_e32 v143, 16, v77
	s_waitcnt vmcnt(30)
	v_lshlrev_b32_e32 v144, 16, v78
	v_cvt_pk_fp8_f32 v20, v39, v45
	s_waitcnt vmcnt(27)
	v_lshlrev_b32_e32 v131, 16, v81
	s_waitcnt vmcnt(26)
	v_lshlrev_b32_e32 v132, 16, v82
	v_and_b32_e32 v81, 0xffff0000, v81
	v_and_b32_e32 v82, 0xffff0000, v82
	v_cvt_pk_fp8_f32 v19, v131, v132
	s_waitcnt vmcnt(23)
	v_lshlrev_b32_e32 v139, 16, v85
	s_waitcnt vmcnt(22)
	v_lshlrev_b32_e32 v140, 16, v86
	v_cvt_pk_fp8_f32 v21, v69, v70
	s_waitcnt vmcnt(19)
	v_lshlrev_b32_e32 v147, 16, v89
	s_waitcnt vmcnt(18)
; __device__ __forceinline__ unsigned pk4_fp8(float a, float b, float c, float d) { unsigned w = 0u; w = __builtin_amdgcn_cvt_pk_fp8_f32(a, b, w, false); w = __builtin_amdgcn_cvt_pk_fp8_f32(c, d, w, true); return w; }
; __device__ __forceinline__ void vt8_transpose(Frame& F) {
;     ...
;         for (int w = 0; w < 16; ++w) { const int k0 = 32 * (w >> 3) + 16 * (w & 1) + 4 * ((w & 7) >> 1);
;             lo[w >> 2][w & 3] = pk4_fp8(bf_lo(v[k0]), bf_lo(v[k0 + 1]), bf_lo(v[k0 + 2]), bf_lo(v[k0 + 3])); hi[w >> 2][w & 3] = pk4_fp8(bf_hi(v[k0]), bf_hi(v[k0 + 1]), bf_hi(v[k0 + 2]), bf_hi(v[k0 + 3])); }
	v_lshlrev_b32_e32 v148, 16, v90
	v_cvt_pk_fp8_f32 v22, v65, v66
	v_cvt_pk_fp8_f32 v23, v81, v82
	v_lshlrev_b32_e32 v42, 16, v33
	v_lshlrev_b32_e32 v43, 16, v38
	v_and_b32_e32 v33, 0xffff0000, v33
	v_and_b32_e32 v38, 0xffff0000, v38
	v_lshlrev_b32_e32 v107, 16, v52
	v_lshlrev_b32_e32 v108, 16, v53
	v_and_b32_e32 v52, 0xffff0000, v52
	v_and_b32_e32 v53, 0xffff0000, v53
	v_lshlrev_b32_e32 v111, 16, v56
	v_lshlrev_b32_e32 v112, 16, v57
	v_and_b32_e32 v56, 0xffff0000, v56
	v_and_b32_e32 v57, 0xffff0000, v57
	v_and_b32_e32 v73, 0xffff0000, v73
	v_and_b32_e32 v74, 0xffff0000, v74
	v_and_b32_e32 v85, 0xffff0000, v85
	v_and_b32_e32 v86, 0xffff0000, v86
	v_and_b32_e32 v77, 0xffff0000, v77
	v_and_b32_e32 v78, 0xffff0000, v78
	v_and_b32_e32 v89, 0xffff0000, v89
	v_and_b32_e32 v90, 0xffff0000, v90
	v_cvt_pk_fp8_f32 v24, v135, v136
	v_cvt_pk_fp8_f32 v25, v139, v140
	v_cvt_pk_fp8_f32 v26, v143, v144
	v_cvt_pk_fp8_f32 v27, v147, v148
	v_mov_b32_e32 v11, 0
	v_mov_b32_e32 v15, 0
	v_lshlrev_b32_e32 v115, 16, v60
	v_lshlrev_b32_e32 v116, 16, v61
	v_and_b32_e32 v60, 0xffff0000, v60
	v_and_b32_e32 v61, 0xffff0000, v61
	v_lshlrev_b32_e32 v121, 16, v63
	v_lshlrev_b32_e32 v122, 16, v64
	v_lshlrev_b32_e32 v125, 16, v71
	v_lshlrev_b32_e32 v126, 16, v72
	v_lshlrev_b32_e32 v129, 16, v67
	v_lshlrev_b32_e32 v130, 16, v68
	v_lshlrev_b32_e32 v133, 16, v83
	v_lshlrev_b32_e32 v134, 16, v84
	s_waitcnt vmcnt(15)
	v_lshlrev_b32_e32 v151, 16, v91
	s_waitcnt vmcnt(14)
	v_lshlrev_b32_e32 v152, 16, v92
	v_and_b32_e32 v91, 0xffff0000, v91
	v_and_b32_e32 v92, 0xffff0000, v92
	v_cvt_pk_fp8_f32 v5, v33, v38
	s_waitcnt vmcnt(11)
	v_lshlrev_b32_e32 v33, 16, v95
	s_waitcnt vmcnt(10)
	v_lshlrev_b32_e32 v38, 16, v96
	v_and_b32_e32 v95, 0xffff0000, v95
	v_and_b32_e32 v96, 0xffff0000, v96
	v_cvt_pk_fp8_f32 v7, v52, v53
	s_waitcnt vmcnt(7)
	v_lshlrev_b32_e32 v52, 16, v99
	s_waitcnt vmcnt(6)
	v_lshlrev_b32_e32 v53, 16, v100
	v_and_b32_e32 v99, 0xffff0000, v99
	v_and_b32_e32 v100, 0xffff0000, v100
	v_cvt_pk_fp8_f32 v13, v56, v57
	s_waitcnt vmcnt(3)
	v_lshlrev_b32_e32 v56, 16, v103
	s_waitcnt vmcnt(2)
; #define GAS __attribute__((address_space(1)))
; __device__ __forceinline__ unsigned pk4_fp8(float a, float b, float c, float d) { unsigned w = 0u; w = __builtin_amdgcn_cvt_pk_fp8_f32(a, b, w, false); w = __builtin_amdgcn_cvt_pk_fp8_f32(c, d, w, true); return w; }
; __device__ __forceinline__ void vt8_transpose(Frame& F) {
;     ...
; #pragma unroll
;         for (int w = 0; w < 16; ++w) { const int k0 = 32 * (w >> 3) + 16 * (w & 1) + 4 * ((w & 7) >> 1);
;             lo[w >> 2][w & 3] = pk4_fp8(bf_lo(v[k0]), bf_lo(v[k0 + 1]), bf_lo(v[k0 + 2]), bf_lo(v[k0 + 3])); hi[w >> 2][w & 3] = pk4_fp8(bf_hi(v[k0]), bf_hi(v[k0 + 1]), bf_hi(v[k0 + 2]), bf_hi(v[k0 + 3])); }
;         GAS u32x4* dst = (GAS u32x4*)(VT + (size_t)blk * 8192 + (size_t)(2 * F.lane) * 64);
; #pragma unroll
;         for (int j = 0; j < 4; ++j) { dst[j] = lo[j]; dst[4 + j] = hi[j]; }
	v_lshlrev_b32_e32 v57, 16, v48
	v_and_b32_e32 v103, 0xffff0000, v103
	v_and_b32_e32 v48, 0xffff0000, v48
	v_cvt_pk_fp8_f32 v28, v73, v74
	v_cvt_pk_fp8_f32 v29, v85, v86
	v_cvt_pk_fp8_f32 v30, v77, v78
	v_cvt_pk_fp8_f32 v31, v89, v90
	v_and_b32_e32 v63, 0xffff0000, v63
	v_and_b32_e32 v64, 0xffff0000, v64
	v_and_b32_e32 v71, 0xffff0000, v71
	v_and_b32_e32 v72, 0xffff0000, v72
	v_and_b32_e32 v67, 0xffff0000, v67
	v_and_b32_e32 v68, 0xffff0000, v68
	v_and_b32_e32 v83, 0xffff0000, v83
	v_and_b32_e32 v84, 0xffff0000, v84
	v_cvt_pk_fp8_f32 v1, v42, v43
	v_cvt_pk_fp8_f32 v3, v107, v108
	v_cvt_pk_fp8_f32 v9, v111, v112
	v_cvt_pk_fp8_f32 v11, v115, v116
	v_cvt_pk_fp8_f32 v15, v60, v61
	v_cvt_pk_fp8_f32 v0, v151, v152
	v_cvt_pk_fp8_f32 v4, v91, v92
	v_cvt_pk_fp8_f32 v2, v33, v38
	v_cvt_pk_fp8_f32 v6, v95, v96
	v_cvt_pk_fp8_f32 v8, v52, v53
	v_cvt_pk_fp8_f32 v12, v99, v100
	v_cvt_pk_fp8_f32 v10, v56, v57
	v_cvt_pk_fp8_f32 v14, v103, v48
	v_cvt_pk_fp8_f32 v16, v121, v122 op_sel:[0,0,1]
	v_cvt_pk_fp8_f32 v17, v125, v126 op_sel:[0,0,1]
	v_cvt_pk_fp8_f32 v18, v129, v130 op_sel:[0,0,1]
	v_cvt_pk_fp8_f32 v19, v133, v134 op_sel:[0,0,1]
	v_lshl_add_u64 v[40:41], s[28:29], 0, v[34:35]
	v_lshlrev_b32_e32 v137, 16, v75
	v_lshlrev_b32_e32 v138, 16, v76
	v_lshlrev_b32_e32 v141, 16, v87
	v_lshlrev_b32_e32 v142, 16, v88
	v_lshlrev_b32_e32 v145, 16, v79
	v_lshlrev_b32_e32 v146, 16, v80
	v_lshlrev_b32_e32 v149, 16, v46
	v_lshlrev_b32_e32 v150, 16, v47
	v_cvt_pk_fp8_f32 v20, v63, v64 op_sel:[0,0,1]
	v_cvt_pk_fp8_f32 v21, v71, v72 op_sel:[0,0,1]
	v_cvt_pk_fp8_f32 v22, v67, v68 op_sel:[0,0,1]
	v_cvt_pk_fp8_f32 v23, v83, v84 op_sel:[0,0,1]
	s_add_i32 s4, s4, s6
	v_add_co_u32_e64 v40, s[2:3], s15, v40
	v_and_b32_e32 v75, 0xffff0000, v75
	v_and_b32_e32 v76, 0xffff0000, v76
	v_and_b32_e32 v87, 0xffff0000, v87
	v_and_b32_e32 v88, 0xffff0000, v88
	v_and_b32_e32 v79, 0xffff0000, v79
	v_and_b32_e32 v80, 0xffff0000, v80
	v_and_b32_e32 v46, 0xffff0000, v46
	v_and_b32_e32 v47, 0xffff0000, v47
	v_cvt_pk_fp8_f32 v24, v137, v138 op_sel:[0,0,1]
	v_cvt_pk_fp8_f32 v25, v141, v142 op_sel:[0,0,1]
	v_cvt_pk_fp8_f32 v26, v145, v146 op_sel:[0,0,1]
	v_cvt_pk_fp8_f32 v27, v149, v150 op_sel:[0,0,1]
	v_lshl_add_u64 v[34:35], v[34:35], 0, s[10:11]
	v_lshl_add_u64 v[36:37], v[36:37], 0, s[12:13]
	v_addc_co_u32_e64 v41, s[2:3], 0, v41, s[2:3]
	s_cmpk_lt_i32 s4, 0x800
	v_lshlrev_b32_e32 v105, 16, v50
	v_lshlrev_b32_e32 v106, 16, v51
	v_and_b32_e32 v50, 0xffff0000, v50
	v_and_b32_e32 v51, 0xffff0000, v51
	v_lshlrev_b32_e32 v109, 16, v54
	v_lshlrev_b32_e32 v110, 16, v55
	v_and_b32_e32 v54, 0xffff0000, v54
	v_and_b32_e32 v55, 0xffff0000, v55
	v_lshlrev_b32_e32 v113, 16, v58
	v_lshlrev_b32_e32 v114, 16, v59
	v_and_b32_e32 v58, 0xffff0000, v58
	v_and_b32_e32 v59, 0xffff0000, v59
	v_lshlrev_b32_e32 v117, 16, v62
	v_lshlrev_b32_e32 v118, 16, v44
	v_and_b32_e32 v62, 0xffff0000, v62
	v_and_b32_e32 v44, 0xffff0000, v44
	v_lshlrev_b32_e32 v153, 16, v93
	v_lshlrev_b32_e32 v154, 16, v94
	v_and_b32_e32 v93, 0xffff0000, v93
	v_and_b32_e32 v94, 0xffff0000, v94
	v_lshlrev_b32_e32 v42, 16, v97
	v_lshlrev_b32_e32 v43, 16, v98
	v_and_b32_e32 v97, 0xffff0000, v97
	v_and_b32_e32 v98, 0xffff0000, v98
	v_lshlrev_b32_e32 v107, 16, v101
	v_lshlrev_b32_e32 v108, 16, v102
	v_and_b32_e32 v101, 0xffff0000, v101
	v_and_b32_e32 v102, 0xffff0000, v102
	s_waitcnt vmcnt(1)
	v_lshlrev_b32_e32 v111, 16, v49
	s_waitcnt vmcnt(0)
	v_lshlrev_b32_e32 v112, 16, v104
	v_and_b32_e32 v49, 0xffff0000, v49
	v_and_b32_e32 v104, 0xffff0000, v104
	v_cvt_pk_fp8_f32 v28, v75, v76 op_sel:[0,0,1]
	v_cvt_pk_fp8_f32 v29, v87, v88 op_sel:[0,0,1]
	v_cvt_pk_fp8_f32 v30, v79, v80 op_sel:[0,0,1]
	v_cvt_pk_fp8_f32 v31, v46, v47 op_sel:[0,0,1]
	v_cvt_pk_fp8_f32 v1, v105, v106 op_sel:[0,0,1]
	v_cvt_pk_fp8_f32 v5, v50, v51 op_sel:[0,0,1]
	v_cvt_pk_fp8_f32 v3, v109, v110 op_sel:[0,0,1]
	v_cvt_pk_fp8_f32 v7, v54, v55 op_sel:[0,0,1]
	v_cvt_pk_fp8_f32 v9, v113, v114 op_sel:[0,0,1]
	v_cvt_pk_fp8_f32 v13, v58, v59 op_sel:[0,0,1]
	v_cvt_pk_fp8_f32 v11, v117, v118 op_sel:[0,0,1]
	v_cvt_pk_fp8_f32 v15, v62, v44 op_sel:[0,0,1]
	v_cvt_pk_fp8_f32 v0, v153, v154 op_sel:[0,0,1]
	v_cvt_pk_fp8_f32 v4, v93, v94 op_sel:[0,0,1]
	v_cvt_pk_fp8_f32 v2, v42, v43 op_sel:[0,0,1]
	v_cvt_pk_fp8_f32 v6, v97, v98 op_sel:[0,0,1]
	v_cvt_pk_fp8_f32 v8, v107, v108 op_sel:[0,0,1]
	v_cvt_pk_fp8_f32 v12, v101, v102 op_sel:[0,0,1]
	v_cvt_pk_fp8_f32 v10, v111, v112 op_sel:[0,0,1]
	v_cvt_pk_fp8_f32 v14, v49, v104 op_sel:[0,0,1]
	global_store_dwordx2 v[40:41], v[0:1], off
	global_store_dwordx2 v[40:41], v[16:17], off offset:8
	global_store_dwordx2 v[40:41], v[2:3], off offset:16
	global_store_dwordx2 v[40:41], v[18:19], off offset:24
	global_store_dwordx2 v[40:41], v[8:9], off offset:32
	global_store_dwordx2 v[40:41], v[24:25], off offset:40
	global_store_dwordx2 v[40:41], v[10:11], off offset:48
	global_store_dwordx2 v[40:41], v[26:27], off offset:56
	global_store_dwordx2 v[40:41], v[4:5], off offset:64
	global_store_dwordx2 v[40:41], v[20:21], off offset:72
	global_store_dwordx2 v[40:41], v[6:7], off offset:80
	global_store_dwordx2 v[40:41], v[22:23], off offset:88
	global_store_dwordx2 v[40:41], v[12:13], off offset:96
	global_store_dwordx2 v[40:41], v[28:29], off offset:104
	global_store_dwordx2 v[40:41], v[14:15], off offset:112
	global_store_dwordx2 v[40:41], v[30:31], off offset:120
	s_cbranch_scc1 .LBB0_1426

; #define LAS __attribute__((address_space(3)))
; __device__ __forceinline__ void ringS_lane_init(RingSLane& R, int wave, int lane) {
; #pragma unroll
;     for (int k = 0; k < 3; ++k) { const int n = wave + 8 * k; int row, ch; unsigned off;
;         if (n < 9) { const int o = n * 1024 + lane * 16; row = o / K8ST; ch = (o % K8ST) >> 4; if (ch > 7) ch = 7; if (row > 63) row = 63; off = (unsigned)(row * 128 + ch * 16); }
;         else { const int o = (n - 9) * 1024 + lane * 16; row = o / VT8ST; ch = (o % VT8ST) >> 4; if (ch > 3) ch = 3; if (row > 127) row = 127; off = (unsigned)(row * 64 + ch * 16); }
;         R.so[k] = off; }
; }
; template <bool DUMMY> __device__ __forceinline__ void sel_phase(Frame& F) {
;     const bf16* Q = (const bf16*)(F.ws + SC_Q); const char* KS = (const char*)(F.ws + SC_KV + 2 * KVS);        const char* VS = (const char*)(F.ws + SC_KV + 1 * KVS);
;     bf16* OW = (bf16*)(F.ws + SC_OW); const float* gates = (const float*)(F.ws + SM_GATES); const unsigned long long* SELM = (const unsigned long long*)(F.ws + SM_SELM);
;     const int lane = F.lane, c = lane & 15, kq = lane >> 4;
;     LAS unsigned long long* Ml = (LAS unsigned long long*)(F.lds + RING_ML_OFF);
;     LAS unsigned short* Lst = (LAS unsigned short*)(F.lds + RING_LIST_OFF); LAS unsigned* Wc = (LAS unsigned*)(F.lds + RING_LIST_OFF + 512);
;     LAS u32x2* PD = (LAS u32x2*)(F.lds + 6 * SLOTS);
;     const int vtlane = c * VT8ST + 8 * kq; const int klane = c * K8ST + 32 * kq;
;     RingSLane RL; ringS_lane_init(RL, F.wave, lane);
;     int it = 0;
;     for (int unit = F.vcu; unit < 2048; unit += F.G, ++it) {
;         const int bh = unit >> 8, tl = unit & 255, tile = (it & 1) ? 255 - tl : tl, b = bh >> 2, kvh = bh & 3, t0 = tile * 64, cur = tile;
;         const int tokA = t0 + 8 * F.wave + (c >> 2), head = kvh * GQ + (c & 3);
;         const size_t qoff = ((size_t)(b * NH + head) * SEQ + tokA) * HD;
;         GS8 g0, g1; gs8_init(g0, Q + qoff + 32 * kq); gs8_init(g1, Q + qoff + 4 * HD + 32 * kq);
;         unsigned long long mym = 0ull; if (F.tid < 256) { mym = SELM[(size_t)(bh * 256 + tile) * 256 + F.tid]; Ml[F.tid] = mym; }
.LBB0_1699:
	s_cmpk_gt_i32 s77, 0x7ff
	s_cbranch_scc1 .LBB0_1817
	s_add_u32 s22, s28, 0x1a000000
	s_addc_u32 s23, s29, 0
	s_add_u32 s78, s28, 0x26000000
	s_addc_u32 s79, s29, 0
	s_add_u32 s80, s28, 0x24000000
	s_addc_u32 s81, s29, 0
	s_add_u32 s24, s28, 0x2e000000
	v_writelane_b32 v238, s90, 7
	s_addc_u32 s25, s29, 0
	v_add_u32_e32 v0, s8, v0
	v_writelane_b32 v238, s92, 3
	s_add_u32 s42, s28, 0xe40000
	v_add_u32_e32 v0, 0x4000, v0
	s_mov_b32 s2, 0x66666667
	v_writelane_b32 v238, s93, 4
	s_addc_u32 s43, s29, 0
	v_mul_hi_i32 v1, v0, s2
	s_lshl_b32 s83, s96, 3
	v_writelane_b32 v238, s94, 5
	v_lshrrev_b32_e32 v9, 31, v1
	v_ashrrev_i32_e32 v1, 5, v1
	s_cmpk_gt_u32 s21, 0xff
	v_writelane_b32 v238, s95, 6
	v_add_u32_e32 v1, v1, v9
	s_movk_i32 s10, 0x50
	s_cselect_b64 s[4:5], -1, 0
	v_min_i32_e32 v9, 0x7f, v1
	v_mul_lo_u32 v1, v1, s10
	v_writelane_b32 v238, s4, 8
	s_cmpk_lt_u32 s21, 0x100
	v_sub_u32_e32 v0, v0, v1
	v_cmp_eq_u32_e32 vcc, 0, v2
	v_writelane_b32 v238, s5, 9
	s_cselect_b64 s[4:5], -1, 0
	v_ashrrev_i32_e32 v0, 4, v0
	s_and_b64 s[46:47], s[4:5], vcc
	v_lshlrev_b32_e32 v9, 6, v9
	v_min_i32_e32 v0, 3, v0
	s_bitcmp1_b32 s21, 6
	v_lshl_add_u32 v108, v0, 4, v9
	v_lshlrev_b64 v[0:1], v2, -1
	s_cselect_b64 s[48:49], -1, 0
	s_add_i32 s84, s83, 0
	v_not_b32_e32 v110, v0
	s_movk_i32 s6, 0x80
	v_and_b32_e32 v0, 0xffffff80, v100
	s_add_i32 s84, s84, 0x1c800
	s_add_i32 s85, s8, 0
	v_ashrrev_i32_e32 v101, 31, v100
	v_not_b32_e32 v111, v1
	v_cmp_gt_i32_e64 s[4:5], s6, v100
	v_cmp_eq_u32_e64 s[6:7], s6, v0
	s_cmpk_lt_u32 s21, 0xc0
	v_lshl_add_u64 v[0:1], v[100:101], 3, s[28:29]
	s_mov_b64 s[8:9], 0x1450000
	s_cselect_b64 s[50:51], -1, 0
	v_lshl_add_u64 v[112:113], v[0:1], 0, s[8:9]
	s_add_i32 s8, 0, 0x23000
	v_lshl_add_u32 v101, v100, 3, s8
	s_lshl_b32 s8, s96, 2
	s_add_i32 s88, s8, 0
	v_lshlrev_b32_e32 v0, 1, v100
	s_add_i32 s8, 0, 0x23800
	v_add_u32_e32 v157, s8, v0
	v_lshlrev_b32_e32 v1, 2, v100
	s_add_i32 s8, 0, 0x1a400
	s_add_i32 s12, 0, 0x1a800
	v_ashrrev_i32_e32 v156, 2, v100
	v_add_u32_e32 v158, s8, v1
	s_add_i32 s11, 0, 0x1aa00
	v_add_u32_e32 v165, s12, v1
	v_and_b32_e32 v1, 0x7f, v100
	v_add_u32_e32 v159, s11, v0
	v_lshl_add_u32 v160, v156, 1, s11
	v_lshl_add_u32 v166, v1, 1, s11
	s_add_i32 s11, 0, 0x1ab80
	s_add_i32 s21, s88, 0x23a00
	s_add_i32 s87, s88, 0x1ac80
	s_add_i32 s88, s88, 0x1ac7c
	v_add_u32_e32 v169, s11, v0
	s_add_i32 s11, 0, 0x1ac90
	s_add_u32 s52, s28, 0x3b400000
	v_add_u32_e32 v170, s11, v0
	s_addc_u32 s53, s29, 0
	s_add_i32 s11, s96, -4
	s_lshr_b32 s12, s11, 2
	s_add_i32 s12, s12, 1
	s_and_b32 s34, s96, 0x3fffffc
	s_and_b32 s13, s12, 7
	s_cmp_gt_u32 s11, 27
	s_cselect_b64 s[36:37], -1, 0
	v_writelane_b32 v238, s36, 10
	s_and_b32 s11, s12, 0x7ffffff8
	s_cmp_lg_u32 s13, 0
	v_writelane_b32 v238, s37, 11
	v_writelane_b32 v238, s11, 12
	s_cselect_b64 s[36:37], -1, 0
	v_writelane_b32 v238, s36, 13
	s_cmp_lg_u32 s96, s34
	v_lshl_add_u32 v102, v3, 4, v4
	v_writelane_b32 v238, s37, 14
	v_ashrrev_i32_e32 v4, 4, v2
	v_writelane_b32 v238, s34, 15
	s_cselect_b64 s[34:35], -1, 0
	v_lshlrev_b32_e32 v7, 3, v4
	v_lshlrev_b32_e32 v104, 5, v4
	v_lshlrev_b32_e32 v155, 2, v4
	v_and_b32_e32 v4, -4, v100
	v_writelane_b32 v238, s34, 16
	v_and_b32_e32 v3, 15, v2
	v_and_b32_e32 v153, 3, v2
	v_add_u32_e32 v161, s8, v4
	v_max_i32_e32 v4, 8, v156
	v_writelane_b32 v238, s35, 17
	s_lshl_b32 s11, s13, 4
	v_lshlrev_b32_e32 v0, 3, v2
	v_mul_u32_u24_e32 v8, 0x90, v3
	v_bfe_u32 v152, v2, 2, 2
	v_mov_b32_e32 v17, 0
	s_movk_i32 s2, 0x100
	v_add_u32_e32 v163, v4, v153
	v_writelane_b32 v238, s11, 18
	v_lshl_add_u32 v172, s96, 9, v0
	v_mad_u32_u24 v0, v3, s10, 0
	s_movk_i32 s10, 0x2400
	v_lshl_add_u32 v106, v5, 4, v6
	v_ashrrev_i32_e32 v105, 31, v104
	s_mov_b32 s82, 0
	v_mov_b32_e32 v103, v17
	v_mov_b32_e32 v107, v17
	v_mov_b32_e32 v109, v17
	v_lshlrev_b32_e64 v154, v152, 1
	v_cmp_gt_i32_e64 s[2:3], s2, v100
	s_movk_i32 s86, 0xc0
	v_add_u32_e32 v162, 8, v156
	v_add_u32_e32 v164, -8, v163
	v_cmp_eq_u32_e64 s[8:9], 0, v153
	v_add_u32_e32 v167, 0xffffff80, v100
	v_add_u16_e32 v168, 0xff80, v100
	v_sub_u32_e32 v171, 0, v156
	v_writelane_b32 v238, s96, 19
	v_add3_u32 v173, v0, v7, s10
	v_add_u32_e32 v173, v173, v7
	v_add3_u32 v174, v8, 0, v104
	v_mov_b32_e32 v175, -1
	v_mov_b32_e32 v176, 1
	s_add_i32 s92, 0, 0x1ac88
	s_mov_b32 s93, 0xffff
	s_add_i32 s94, s85, 0x2000
	s_add_i32 s95, s85, 0x4c00
	s_add_i32 s96, s85, 0x6c00
	s_add_i32 s10, s85, 0x8c00
	s_add_i32 s34, s85, 0x9800
	s_add_i32 s35, s85, 0xb800
	s_add_i32 s75, s85, 0xd800
	s_mov_b32 s90, 0xefa18f08
	v_mov_b32_e32 v177, 0x7c7c7c7c
	v_mov_b32_e32 v178, 0x7f7f7f7f
	s_brev_b32 s91, -3
	v_mov_b32_e32 v115, 0x40400000
	v_mov_b32_e32 v179, 0x1a3e0
	v_mov_b32_e32 v180, 0x1000000
	v_mov_b32_e32 v181, 0xff800000
	s_mov_b32 s74, s77
	v_writelane_b32 v238, s10, 20
	s_branch .LBB0_1703

; __device__ __forceinline__ unsigned lds_addr(const LAS void* p) { return (unsigned)(size_t)p; }
; #define RD16(dst, base, off) asm volatile("ds_read_b128 %0, %1 offset:%2" : "=&v"(dst) : "v"(base), "i"(off) : "memory")
; #define LGKM_W(n) asm volatile("s_waitcnt lgkmcnt(" #n ")" ::: "memory"); SBAR()
; #define QK8_MM(T_) do { i32x8a kf; kf.lo = lo[T_]; kf.hi = hi[T_]; s[T_] = __builtin_amdgcn_mfma_scale_f32_16x16x128_f8f6f4(kf, g.q8, (f32x4){c0, c0, c0, c0}, 0, 0, 0, 0x7f7f7f7f, 0, 0x7c7c7c7c); } while (0)
; #define PV8_RD(dt) do { RD8(f.a[dt][0], vb, (dt) * 16 * VT8ST); RD8(f.a[dt][1], vb, (dt) * 16 * VT8ST + 32); } while (0)
; __device__ __forceinline__ void qk8_tile_c(f32x4 (&s)[4], const GS8& g, const unsigned kb  , const float c0  ) {
;     i32x4a lo[4], hi[4];
;     RD16(lo[0], kb, 0); RD16(hi[0], kb, 16); RD16(lo[1], kb, 16 * K8ST); RD16(hi[1], kb, 16 * K8ST + 16);
;     RD16(lo[2], kb, 32 * K8ST); RD16(hi[2], kb, 32 * K8ST + 16); RD16(lo[3], kb, 48 * K8ST); RD16(hi[3], kb, 48 * K8ST + 16);
;     ...
;     LGKM_W(6); QK8_MM(0); LGKM_W(4); QK8_MM(1); LGKM_W(2); QK8_MM(2); LGKM_W(0); QK8_MM(3);
;     ...
; }
; __device__ __forceinline__ void pv8_issue(VT8Frag& f, const unsigned vb  ) {
;     ...
;     PV8_RD(0); PV8_RD(1); PV8_RD(2); PV8_RD(3); PV8_RD(4); PV8_RD(5); PV8_RD(6); PV8_RD(7);
;     ...
; }
; template <bool DUMMY> __device__ __forceinline__ void sel_phase(Frame& F) {
;     ...
;                 const int kb = jc * 64; const bool diag = (jc == cur); f32x4 s0[4], s1[4];
;                 const float bA = selA ? 0.f : NINF, bB = selB ? 0.f : NINF;
;                 if (a0 != 0u) {
;                     const float rf = sm8_ref(g0);
;                     VT8Frag vf; qk8_tile_c(s0, g0, lds_addr(sb) + (unsigned)klane, bA + (5.f - rf)); pv8_issue(vf, lds_addr(sb + K8TB) + (unsigned)vtlane);
;                     if (diag) mask_scores(s0, tokA, 0x40000000u, kb, kq);
;                     online_sm8(s0, g0, rf);
;                     pv8_mm(g0, s0, vf);
.Lsel_nodma:
	s_lshr_b32 s45, s67, s36
	s_and_b32 s97, s45, 0xff
	s_cbranch_scc0 .LBB0_1798
	ds_read_b128 v[84:87], v208 offset:0
	ds_read_b128 v[88:91], v208 offset:16
	ds_read_b128 v[92:95], v208 offset:0x900
	ds_read_b128 v[96:99], v208 offset:0x910
	ds_read_b128 v[118:121], v208 offset:0x1200
	ds_read_b128 v[122:125], v208 offset:0x1210
	s_and_b32 vcc_lo, s45, 15
	s_cbranch_scc0 .Lsel_g1_pre
	v_and_b32_e32 v18, s45, v154
	v_cmp_eq_u32_e32 vcc, 0, v18
	s_lshr_b32 s44, s66, s36
	s_and_b32 s44, s44, 0xff
	v_cndmask_b32_e32 v210, v216, v181, vcc
	v_mov_b32_e32 v211, v210
	v_mov_b32_e32 v212, v210
	v_mov_b32_e32 v213, v210
	ds_read_b128 v[126:129], v208 offset:0x1b00
	ds_read_b128 v[130:133], v208 offset:0x1b10
	s_waitcnt lgkmcnt(6)
	v_mfma_scale_f32_16x16x128_f8f6f4 v[84:87], v[84:91], v[0:7], v[210:213], v178, v177 op_sel_hi:[0,0,0]
	ds_read_b128 v[134:137], v207 offset:0
	ds_read_b128 v[138:141], v207 offset:0x500
	ds_read_b128 v[142:145], v207 offset:0xa00
	ds_read_b128 v[146:149], v207 offset:0xf00
	s_waitcnt lgkmcnt(8)
	v_mfma_scale_f32_16x16x128_f8f6f4 v[88:91], v[92:99], v[0:7], v[210:213], v178, v177 op_sel_hi:[0,0,0]
	s_waitcnt lgkmcnt(6)
	v_mfma_scale_f32_16x16x128_f8f6f4 v[92:95], v[118:125], v[0:7], v[210:213], v178, v177 op_sel_hi:[0,0,0]
	s_waitcnt lgkmcnt(4)
	v_mfma_scale_f32_16x16x128_f8f6f4 v[96:99], v[126:133], v[0:7], v[210:213], v178, v177 op_sel_hi:[0,0,0]
	ds_read_b128 v[118:121], v207 offset:0x1400
	ds_read_b128 v[122:125], v207 offset:0x1900
	ds_read_b128 v[126:129], v207 offset:0x1e00
	ds_read_b128 v[130:133], v207 offset:0x2300
	s_cmp_eq_u32 s44, s58
	s_cbranch_scc1 .Lsel_diag_g0

; __device__ __forceinline__ unsigned pk4_fp8(float a, float b, float c, float d) { unsigned w = 0u; w = __builtin_amdgcn_cvt_pk_fp8_f32(a, b, w, false); w = __builtin_amdgcn_cvt_pk_fp8_f32(c, d, w, true); return w; }
; #define LGKM_W(n) asm volatile("s_waitcnt lgkmcnt(" #n ")" ::: "memory"); SBAR()
; #define PV8_MM(dt) do { g.o[dt] = __builtin_amdgcn_mfma_f32_16x16x32_fp8_fp8(f.a[dt][0], b0, g.o[dt], 0, 0, 0); g.o[dt] = __builtin_amdgcn_mfma_f32_16x16x32_fp8_fp8(f.a[dt][1], b1, g.o[dt], 0, 0, 0); } while (0)
; template <class G> __device__ __forceinline__ void pv8_mm(G& g, const f32x4 (&s)[4], const VT8Frag& f) {
;     ...
;     unsigned pa[4];
; #pragma unroll
;     for (int T_ = 0; T_ < 4; ++T_) pa[T_] = pk4_fp8(s[T_][0], s[T_][1], s[T_][2], s[T_][3]);
;     const long b0 = (long)(((unsigned long long)pa[1] << 32) | pa[0]), b1 = (long)(((unsigned long long)pa[3] << 32) | pa[2]);
;     LGKM_W(14); PV8_MM(0); LGKM_W(12); PV8_MM(1); LGKM_W(10); PV8_MM(2); LGKM_W(8); PV8_MM(3);
;     LGKM_W(6); PV8_MM(4); LGKM_W(4); PV8_MM(5); LGKM_W(2); PV8_MM(6); LGKM_W(0); PV8_MM(7);
;     ...
; }
; template <class G> __device__ __forceinline__ void online_sm8(f32x4 (&s)[4], G& g, const float ref) {
;     ...
;     float ps = 0.f;
; #pragma unroll
;     for (int T_ = 0; T_ < 4; ++T_)
; #pragma unroll
;         for (int i = 0; i < 4; ++i) { s[T_][i] = __builtin_amdgcn_exp2f(s[T_][i]); ps += s[T_][i]; }
;     g.l += ps;
.LBB0_1808:
	v_exp_f32_e32 v240, v84
	v_exp_f32_e32 v241, v85
	v_exp_f32_e32 v242, v86
	v_exp_f32_e32 v243, v87
	v_exp_f32_e32 v244, v88
	v_exp_f32_e32 v245, v89
	v_exp_f32_e32 v246, v90
	v_exp_f32_e32 v247, v91
	s_waitcnt lgkmcnt(0)
	v_cvt_pk_fp8_f32 v84, v240, v241
	v_cvt_pk_fp8_f32 v85, v244, v245
	v_cvt_pk_fp8_f32 v84, v242, v243 op_sel:[0,0,1]
	v_cvt_pk_fp8_f32 v85, v246, v247 op_sel:[0,0,1]
	v_exp_f32_e32 v248, v92
	v_exp_f32_e32 v249, v93
	v_mfma_f32_16x16x32_fp8_fp8 v[80:83], v[134:135], v[84:85], v[80:83]
	v_exp_f32_e32 v250, v94
	v_mfma_f32_16x16x32_fp8_fp8 v[76:79], v[138:139], v[84:85], v[76:79]
	v_exp_f32_e32 v251, v95
	v_mfma_f32_16x16x32_fp8_fp8 v[72:75], v[142:143], v[84:85], v[72:75]
	v_exp_f32_e32 v252, v96
	v_mfma_f32_16x16x32_fp8_fp8 v[68:71], v[146:147], v[84:85], v[68:71]
	v_exp_f32_e32 v253, v97
	v_mfma_f32_16x16x32_fp8_fp8 v[64:67], v[118:119], v[84:85], v[64:67]
	v_exp_f32_e32 v254, v98
	v_mfma_f32_16x16x32_fp8_fp8 v[60:63], v[122:123], v[84:85], v[60:63]
	v_exp_f32_e32 v255, v99
	v_mfma_f32_16x16x32_fp8_fp8 v[56:59], v[126:127], v[84:85], v[56:59]
	v_mfma_f32_16x16x32_fp8_fp8 v[52:55], v[130:131], v[84:85], v[52:55]
	v_cvt_pk_fp8_f32 v86, v248, v249
	v_cvt_pk_fp8_f32 v87, v252, v253
	v_cvt_pk_fp8_f32 v86, v250, v251 op_sel:[0,0,1]
	v_cvt_pk_fp8_f32 v87, v254, v255 op_sel:[0,0,1]
	v_add_f32_e32 v240, v240, v241
	v_add_f32_e32 v242, v242, v243
	v_mfma_f32_16x16x32_fp8_fp8 v[80:83], v[136:137], v[86:87], v[80:83]
	v_add_f32_e32 v244, v244, v245
	v_add_f32_e32 v246, v246, v247
	v_mfma_f32_16x16x32_fp8_fp8 v[76:79], v[140:141], v[86:87], v[76:79]
	v_add_f32_e32 v248, v248, v249
	v_add_f32_e32 v250, v250, v251
	v_mfma_f32_16x16x32_fp8_fp8 v[72:75], v[144:145], v[86:87], v[72:75]
	v_add_f32_e32 v252, v252, v253
	v_add_f32_e32 v254, v254, v255
	v_mfma_f32_16x16x32_fp8_fp8 v[68:71], v[148:149], v[86:87], v[68:71]
	v_add_f32_e32 v240, v240, v242
	v_add_f32_e32 v244, v244, v246
	v_mfma_f32_16x16x32_fp8_fp8 v[64:67], v[120:121], v[86:87], v[64:67]
	v_add_f32_e32 v248, v248, v250
	v_add_f32_e32 v252, v252, v254
	v_mfma_f32_16x16x32_fp8_fp8 v[60:63], v[124:125], v[86:87], v[60:63]
	v_add_f32_e32 v240, v240, v244
	v_add_f32_e32 v248, v248, v252
	v_mfma_f32_16x16x32_fp8_fp8 v[56:59], v[128:129], v[86:87], v[56:59]
	v_add_f32_e32 v240, v240, v248
	v_add_f32_e32 v183, v183, v240
	v_mfma_f32_16x16x32_fp8_fp8 v[52:55], v[132:133], v[86:87], v[52:55]

; __device__ __forceinline__ unsigned lds_addr(const LAS void* p) { return (unsigned)(size_t)p; }
; #define RD16(dst, base, off) asm volatile("ds_read_b128 %0, %1 offset:%2" : "=&v"(dst) : "v"(base), "i"(off) : "memory")
; #define LGKM_W(n) asm volatile("s_waitcnt lgkmcnt(" #n ")" ::: "memory"); SBAR()
; #define QK8_MM(T_) do { i32x8a kf; kf.lo = lo[T_]; kf.hi = hi[T_]; s[T_] = __builtin_amdgcn_mfma_scale_f32_16x16x128_f8f6f4(kf, g.q8, (f32x4){c0, c0, c0, c0}, 0, 0, 0, 0x7f7f7f7f, 0, 0x7c7c7c7c); } while (0)
; #define PV8_RD(dt) do { RD8(f.a[dt][0], vb, (dt) * 16 * VT8ST); RD8(f.a[dt][1], vb, (dt) * 16 * VT8ST + 32); } while (0)
; __device__ __forceinline__ void qk8_tile_c(f32x4 (&s)[4], const GS8& g, const unsigned kb  , const float c0  ) {
;     i32x4a lo[4], hi[4];
;     RD16(lo[0], kb, 0); RD16(hi[0], kb, 16); RD16(lo[1], kb, 16 * K8ST); RD16(hi[1], kb, 16 * K8ST + 16);
;     RD16(lo[2], kb, 32 * K8ST); RD16(hi[2], kb, 32 * K8ST + 16); RD16(lo[3], kb, 48 * K8ST); RD16(hi[3], kb, 48 * K8ST + 16);
;     ...
;     LGKM_W(6); QK8_MM(0); LGKM_W(4); QK8_MM(1); LGKM_W(2); QK8_MM(2); LGKM_W(0); QK8_MM(3);
;     ...
; }
; __device__ __forceinline__ void pv8_issue(VT8Frag& f, const unsigned vb  ) {
;     ...
;     PV8_RD(0); PV8_RD(1); PV8_RD(2); PV8_RD(3); PV8_RD(4); PV8_RD(5); PV8_RD(6); PV8_RD(7);
;     ...
; }
; template <bool DUMMY> __device__ __forceinline__ void sel_phase(Frame& F) {
;     ...
;                 if (a1 != 0u) {
;                     const float rf = sm8_ref(g1);
;                     VT8Frag vf; qk8_tile_c(s0, g1, lds_addr(sb) + (unsigned)klane, bB + (5.f - rf)); pv8_issue(vf, lds_addr(sb + K8TB) + (unsigned)vtlane);
;                     if (diag) mask_scores(s0, tokA + 4, 0x40000000u, kb, kq);
;                     online_sm8(s0, g1, rf);
;                     pv8_mm(g1, s0, vf);
.Lsel_g1_pre:
	s_lshr_b32 s45, s45, 4
	v_and_b32_e32 v18, s45, v154
	v_cmp_eq_u32_e32 vcc, 0, v18
	s_lshr_b32 s44, s66, s36
	s_and_b32 s44, s44, 0xff
	v_cndmask_b32_e32 v210, v220, v181, vcc
	v_mov_b32_e32 v211, v210
	v_mov_b32_e32 v212, v210
	v_mov_b32_e32 v213, v210
	ds_read_b128 v[126:129], v208 offset:0x1b00
	ds_read_b128 v[130:133], v208 offset:0x1b10
	s_waitcnt lgkmcnt(6)
	v_mfma_scale_f32_16x16x128_f8f6f4 v[84:87], v[84:91], v[8:15], v[210:213], v178, v177 op_sel_hi:[0,0,0]
	ds_read_b128 v[134:137], v207 offset:0
	ds_read_b128 v[138:141], v207 offset:0x500
	ds_read_b128 v[142:145], v207 offset:0xa00
	ds_read_b128 v[146:149], v207 offset:0xf00
	s_waitcnt lgkmcnt(8)
	v_mfma_scale_f32_16x16x128_f8f6f4 v[88:91], v[92:99], v[8:15], v[210:213], v178, v177 op_sel_hi:[0,0,0]
	s_waitcnt lgkmcnt(6)
	v_mfma_scale_f32_16x16x128_f8f6f4 v[92:95], v[118:125], v[8:15], v[210:213], v178, v177 op_sel_hi:[0,0,0]
	s_waitcnt lgkmcnt(4)
	v_mfma_scale_f32_16x16x128_f8f6f4 v[96:99], v[126:133], v[8:15], v[210:213], v178, v177 op_sel_hi:[0,0,0]
	ds_read_b128 v[118:121], v207 offset:0x1400
	ds_read_b128 v[122:125], v207 offset:0x1900
	ds_read_b128 v[126:129], v207 offset:0x1e00
	ds_read_b128 v[130:133], v207 offset:0x2300
	s_cmp_eq_u32 s44, s58
	s_cbranch_scc1 .Lsel_diag_g1

; __device__ __forceinline__ unsigned pk4_fp8(float a, float b, float c, float d) { unsigned w = 0u; w = __builtin_amdgcn_cvt_pk_fp8_f32(a, b, w, false); w = __builtin_amdgcn_cvt_pk_fp8_f32(c, d, w, true); return w; }
; #define LGKM_W(n) asm volatile("s_waitcnt lgkmcnt(" #n ")" ::: "memory"); SBAR()
; #define PV8_MM(dt) do { g.o[dt] = __builtin_amdgcn_mfma_f32_16x16x32_fp8_fp8(f.a[dt][0], b0, g.o[dt], 0, 0, 0); g.o[dt] = __builtin_amdgcn_mfma_f32_16x16x32_fp8_fp8(f.a[dt][1], b1, g.o[dt], 0, 0, 0); } while (0)
; template <class G> __device__ __forceinline__ void pv8_mm(G& g, const f32x4 (&s)[4], const VT8Frag& f) {
;     ...
;     unsigned pa[4];
; #pragma unroll
;     for (int T_ = 0; T_ < 4; ++T_) pa[T_] = pk4_fp8(s[T_][0], s[T_][1], s[T_][2], s[T_][3]);
;     const long b0 = (long)(((unsigned long long)pa[1] << 32) | pa[0]), b1 = (long)(((unsigned long long)pa[3] << 32) | pa[2]);
;     LGKM_W(14); PV8_MM(0); LGKM_W(12); PV8_MM(1); LGKM_W(10); PV8_MM(2); LGKM_W(8); PV8_MM(3);
;     LGKM_W(6); PV8_MM(4); LGKM_W(4); PV8_MM(5); LGKM_W(2); PV8_MM(6); LGKM_W(0); PV8_MM(7);
;     ...
; }
; template <class G> __device__ __forceinline__ void online_sm8(f32x4 (&s)[4], G& g, const float ref) {
;     ...
;     float ps = 0.f;
; #pragma unroll
;     for (int T_ = 0; T_ < 4; ++T_)
; #pragma unroll
;         for (int i = 0; i < 4; ++i) { s[T_][i] = __builtin_amdgcn_exp2f(s[T_][i]); ps += s[T_][i]; }
;     g.l += ps;
.LBB0_1797:
	v_exp_f32_e32 v240, v84
	v_exp_f32_e32 v241, v85
	v_exp_f32_e32 v242, v86
	v_exp_f32_e32 v243, v87
	v_exp_f32_e32 v244, v88
	v_exp_f32_e32 v245, v89
	v_exp_f32_e32 v246, v90
	v_exp_f32_e32 v247, v91
	s_waitcnt lgkmcnt(0)
	v_cvt_pk_fp8_f32 v84, v240, v241
	v_cvt_pk_fp8_f32 v85, v244, v245
	v_cvt_pk_fp8_f32 v84, v242, v243 op_sel:[0,0,1]
	v_cvt_pk_fp8_f32 v85, v246, v247 op_sel:[0,0,1]
	v_exp_f32_e32 v248, v92
	v_exp_f32_e32 v249, v93
	v_mfma_f32_16x16x32_fp8_fp8 v[48:51], v[134:135], v[84:85], v[48:51]
	v_exp_f32_e32 v250, v94
	v_mfma_f32_16x16x32_fp8_fp8 v[44:47], v[138:139], v[84:85], v[44:47]
	v_exp_f32_e32 v251, v95
	v_mfma_f32_16x16x32_fp8_fp8 v[40:43], v[142:143], v[84:85], v[40:43]
	v_exp_f32_e32 v252, v96
	v_mfma_f32_16x16x32_fp8_fp8 v[36:39], v[146:147], v[84:85], v[36:39]
	v_exp_f32_e32 v253, v97
	v_mfma_f32_16x16x32_fp8_fp8 v[32:35], v[118:119], v[84:85], v[32:35]
	v_exp_f32_e32 v254, v98
	v_mfma_f32_16x16x32_fp8_fp8 v[28:31], v[122:123], v[84:85], v[28:31]
	v_exp_f32_e32 v255, v99
	v_mfma_f32_16x16x32_fp8_fp8 v[24:27], v[126:127], v[84:85], v[24:27]
	v_mfma_f32_16x16x32_fp8_fp8 v[20:23], v[130:131], v[84:85], v[20:23]
	v_cvt_pk_fp8_f32 v86, v248, v249
	v_cvt_pk_fp8_f32 v87, v252, v253
	v_cvt_pk_fp8_f32 v86, v250, v251 op_sel:[0,0,1]
	v_cvt_pk_fp8_f32 v87, v254, v255 op_sel:[0,0,1]
	v_add_f32_e32 v240, v240, v241
	v_add_f32_e32 v242, v242, v243
	v_mfma_f32_16x16x32_fp8_fp8 v[48:51], v[136:137], v[86:87], v[48:51]
	v_add_f32_e32 v244, v244, v245
	v_add_f32_e32 v246, v246, v247
	v_mfma_f32_16x16x32_fp8_fp8 v[44:47], v[140:141], v[86:87], v[44:47]
	v_add_f32_e32 v248, v248, v249
	v_add_f32_e32 v250, v250, v251
	v_mfma_f32_16x16x32_fp8_fp8 v[40:43], v[144:145], v[86:87], v[40:43]
	v_add_f32_e32 v252, v252, v253
	v_add_f32_e32 v254, v254, v255
	v_mfma_f32_16x16x32_fp8_fp8 v[36:39], v[148:149], v[86:87], v[36:39]
	v_add_f32_e32 v240, v240, v242
	v_add_f32_e32 v244, v244, v246
	v_mfma_f32_16x16x32_fp8_fp8 v[32:35], v[120:121], v[86:87], v[32:35]
	v_add_f32_e32 v248, v248, v250
	v_add_f32_e32 v252, v252, v254
	v_mfma_f32_16x16x32_fp8_fp8 v[28:31], v[124:125], v[86:87], v[28:31]
	v_add_f32_e32 v240, v240, v244
	v_add_f32_e32 v248, v248, v252
	v_mfma_f32_16x16x32_fp8_fp8 v[24:27], v[128:129], v[86:87], v[24:27]
	v_add_f32_e32 v240, v240, v248
	v_add_f32_e32 v182, v182, v240
	v_mfma_f32_16x16x32_fp8_fp8 v[20:23], v[132:133], v[86:87], v[20:23]
	s_branch .LBB0_1798
